# gdn_scan: u0-load / output-store addresses formed by one v_lshl_add_u64 (constant in s[26:27]) instead of a 4-slot carry chain in the MFMA gaps, on top of v95
# baseline (speedup 1.0000x reference)
.LBB0_490:
	s_bitcmp1_b32 s35, 0
	s_cselect_b32 s26, 0xea00, 0
	v_add_u32_e32 v159, s26, v157
	v_add_u32_e32 v190, v159, v155
	ds_read2_b64 v[68:71], v190 offset1:2
	ds_read2_b64 v[84:87], v190 offset0:4 offset1:6
	ds_read2_b64 v[88:91], v190 offset0:8 offset1:10
	ds_read2_b64 v[92:95], v190 offset0:12 offset1:14
	ds_read2_b64 v[96:99], v190 offset0:16 offset1:18
	ds_read2_b64 v[100:103], v190 offset0:20 offset1:22
	ds_read2_b64 v[104:107], v190 offset0:24 offset1:26
	ds_read2_b64 v[108:111], v190 offset0:28 offset1:30
	v_add_u32_e32 v112, 0x2000, v190
	v_add_u32_e32 v182, 0x2000, v190
	v_add_u32_e32 v186, 0x2000, v190
	v_add_u32_e32 v214, 0x2000, v190
	ds_read2_b64 v[112:115], v112 offset0:48 offset1:50
	ds_read2_b64 v[182:185], v182 offset0:52 offset1:54
	ds_read2_b64 v[186:189], v186 offset0:56 offset1:58
	ds_read2_b64 v[214:217], v214 offset0:60 offset1:62
	v_cvt_pk_bf16_f32 v116, v52, v53
	v_cvt_pk_bf16_f32 v117, v54, v55
	v_cvt_pk_bf16_f32 v118, v56, v57
	v_cvt_pk_bf16_f32 v119, v58, v59
	v_cvt_pk_bf16_f32 v120, v60, v61
	v_cvt_pk_bf16_f32 v121, v62, v63
	v_cvt_pk_bf16_f32 v122, v64, v65
	v_cvt_pk_bf16_f32 v123, v66, v67
	v_cvt_pk_bf16_f32 v124, v36, v37
	v_cvt_pk_bf16_f32 v125, v38, v39
	v_cvt_pk_bf16_f32 v126, v40, v41
	v_cvt_pk_bf16_f32 v127, v42, v43
	v_cvt_pk_bf16_f32 v128, v44, v45
	v_cvt_pk_bf16_f32 v129, v46, v47
	v_cvt_pk_bf16_f32 v130, v48, v49
	v_cvt_pk_bf16_f32 v131, v50, v51
	v_cvt_pk_bf16_f32 v132, v20, v21
	v_cvt_pk_bf16_f32 v133, v22, v23
	v_cvt_pk_bf16_f32 v134, v24, v25
	v_cvt_pk_bf16_f32 v135, v26, v27
	v_cvt_pk_bf16_f32 v136, v28, v29
	v_cvt_pk_bf16_f32 v137, v30, v31
	v_cvt_pk_bf16_f32 v138, v32, v33
	v_cvt_pk_bf16_f32 v139, v34, v35
	v_cvt_pk_bf16_f32 v140, v4, v5
	v_cvt_pk_bf16_f32 v141, v6, v7
	v_cvt_pk_bf16_f32 v142, v8, v9
	v_cvt_pk_bf16_f32 v143, v10, v11
	v_cvt_pk_bf16_f32 v144, v12, v13
	v_cvt_pk_bf16_f32 v145, v14, v15
	v_cvt_pk_bf16_f32 v146, v16, v17
	v_cvt_pk_bf16_f32 v147, v18, v19
	s_waitcnt lgkmcnt(4)
	v_mfma_f32_32x32x16_bf16 v[68:83], v[68:71], v[116:119], 0
	v_mfma_f32_32x32x16_bf16 v[68:83], v[84:87], v[120:123], v[68:83]
	v_add_u32_e32 v84, 0x2000, v190
	ds_read2_b64 v[84:87], v84 offset0:32 offset1:34
	v_mfma_f32_32x32x16_bf16 v[68:83], v[88:91], v[124:127], v[68:83]
	v_mfma_f32_32x32x16_bf16 v[68:83], v[92:95], v[128:131], v[68:83]
	v_mfma_f32_32x32x16_bf16 v[68:83], v[96:99], v[132:135], v[68:83]
	v_mfma_f32_32x32x16_bf16 v[68:83], v[100:103], v[136:139], v[68:83]
	v_add_u32_e32 v100, 0x2000, v190
	ds_read2_b64 v[100:103], v100 offset0:36 offset1:38
	v_mfma_f32_32x32x16_bf16 v[68:83], v[104:107], v[140:143], v[68:83]
	v_add_u32_e32 v104, 0x2000, v190
	ds_read2_b64 v[104:107], v104 offset0:40 offset1:42
	v_mfma_f32_32x32x16_bf16 v[68:83], v[108:111], v[144:147], v[68:83]
	v_add_u32_e32 v108, 0x2000, v190
	ds_read2_b64 v[108:111], v108 offset0:44 offset1:46
	v_add_u32_e32 v88, 0x2000, v190
	s_waitcnt lgkmcnt(3)
	v_mfma_f32_32x32x16_bf16 v[84:99], v[84:87], v[116:119], 0
	s_waitcnt lgkmcnt(2)
	v_mfma_f32_32x32x16_bf16 v[84:99], v[100:103], v[120:123], v[84:99]
	s_waitcnt lgkmcnt(1)
	v_mfma_f32_32x32x16_bf16 v[84:99], v[104:107], v[124:127], v[84:99]
	s_waitcnt lgkmcnt(0)
	v_mfma_f32_32x32x16_bf16 v[84:99], v[108:111], v[128:131], v[84:99]
	v_mfma_f32_32x32x16_bf16 v[84:99], v[112:115], v[132:135], v[84:99]
	v_mfma_f32_32x32x16_bf16 v[84:99], v[182:185], v[136:139], v[84:99]
	v_mfma_f32_32x32x16_bf16 v[84:99], v[186:189], v[140:143], v[84:99]
	v_mfma_f32_32x32x16_bf16 v[84:99], v[214:217], v[144:147], v[84:99]
	s_waitcnt vmcnt(32)
	v_mov_b32_e32 v200, v201
	v_sub_f32_e32 v81, v197, v81
	v_sub_f32_e32 v80, v196, v80
	v_sub_f32_e32 v71, v165, v71
	v_sub_f32_e32 v70, v164, v70
	v_sub_f32_e32 v69, v167, v69
	v_sub_f32_e32 v68, v166, v68
	v_cvt_pk_bf16_f32 v106, v80, v81
	s_nop 3
	v_sub_f32_e32 v80, v175, v87
	v_sub_f32_e32 v81, v174, v86
	v_sub_f32_e32 v83, v199, v83
	v_sub_f32_e32 v82, v198, v82
	v_sub_f32_e32 v79, v195, v79
	v_sub_f32_e32 v78, v194, v78
	v_sub_f32_e32 v77, v181, v77
	v_sub_f32_e32 v76, v180, v76
	v_sub_f32_e32 v75, v171, v75
	v_sub_f32_e32 v74, v170, v74
	v_sub_f32_e32 v73, v169, v73
	v_sub_f32_e32 v72, v168, v72
	v_cvt_pk_bf16_f32 v100, v68, v69
	v_cvt_pk_bf16_f32 v101, v70, v71
	v_sub_f32_e32 v68, v179, v91
	v_sub_f32_e32 v69, v178, v90
	v_sub_f32_e32 v70, v177, v89
	v_sub_f32_e32 v71, v176, v88
	v_cvt_pk_bf16_f32 v109, v81, v80
	v_add_u32_e32 v80, 0x4000, v190
	v_cvt_pk_bf16_f32 v102, v72, v73
	v_cvt_pk_bf16_f32 v103, v74, v75
	v_cvt_pk_bf16_f32 v104, v76, v77
	v_cvt_pk_bf16_f32 v105, v78, v79
	v_cvt_pk_bf16_f32 v107, v82, v83
	v_sub_f32_e32 v72, v209, v99
	v_sub_f32_e32 v73, v208, v98
	v_sub_f32_e32 v74, v207, v97
	v_sub_f32_e32 v75, v206, v96
	v_sub_f32_e32 v76, v205, v95
	v_sub_f32_e32 v77, v204, v94
	v_sub_f32_e32 v78, v203, v93
	v_sub_f32_e32 v79, v202, v92
	v_sub_f32_e32 v82, v173, v85
	v_sub_f32_e32 v83, v172, v84
	v_cvt_pk_bf16_f32 v110, v71, v70
	v_cvt_pk_bf16_f32 v111, v69, v68
	ds_read2_b64 v[68:71], v80 offset0:64 offset1:66
	ds_read2_b64 v[84:87], v80 offset0:68 offset1:70
	ds_read2_b64 v[88:91], v80 offset0:72 offset1:74
	ds_read2_b64 v[92:95], v80 offset0:76 offset1:78
	ds_read2_b64 v[96:99], v80 offset0:80 offset1:82
	ds_read2_b64 v[164:167], v80 offset0:84 offset1:86
	ds_read2_b64 v[168:171], v80 offset0:88 offset1:90
	ds_read2_b64 v[172:175], v80 offset0:92 offset1:94
	v_add_u32_e32 v176, 0x6000, v190
	v_add_u32_e32 v180, 0x6000, v190
	v_add_u32_e32 v184, 0x6000, v190
	v_add_u32_e32 v194, 0x6000, v190
	ds_read2_b64 v[176:179], v176 offset0:112 offset1:114
	ds_read2_b64 v[180:183], v180 offset0:116 offset1:118
	ds_read2_b64 v[184:187], v184 offset0:120 offset1:122
	ds_read2_b64 v[194:197], v194 offset0:124 offset1:126
	v_cvt_pk_bf16_f32 v108, v83, v82
	v_cvt_pk_bf16_f32 v112, v79, v78
	v_cvt_pk_bf16_f32 v113, v77, v76
	v_cvt_pk_bf16_f32 v114, v75, v74
	v_cvt_pk_bf16_f32 v115, v73, v72
	s_waitcnt lgkmcnt(11)
	v_mfma_f32_32x32x16_bf16 v[68:83], v[68:71], v[116:119], 0
	s_waitcnt lgkmcnt(10)
	v_mfma_f32_32x32x16_bf16 v[68:83], v[84:87], v[120:123], v[68:83]
	v_add_u32_e32 v84, 0x6000, v190
	ds_read2_b64 v[84:87], v84 offset0:96 offset1:98
	s_waitcnt lgkmcnt(10)
	v_mfma_f32_32x32x16_bf16 v[68:83], v[88:91], v[124:127], v[68:83]
	s_waitcnt lgkmcnt(9)
	v_mfma_f32_32x32x16_bf16 v[68:83], v[92:95], v[128:131], v[68:83]
	s_waitcnt lgkmcnt(8)
	v_mfma_f32_32x32x16_bf16 v[68:83], v[96:99], v[132:135], v[68:83]
	s_waitcnt lgkmcnt(7)
	v_mfma_f32_32x32x16_bf16 v[68:83], v[164:167], v[136:139], v[68:83]
	v_add_u32_e32 v164, 0x6000, v190
	ds_read2_b64 v[164:167], v164 offset0:100 offset1:102
	s_waitcnt lgkmcnt(7)
	v_mfma_f32_32x32x16_bf16 v[68:83], v[168:171], v[140:143], v[68:83]
	v_add_u32_e32 v168, 0x6000, v190
	ds_read2_b64 v[168:171], v168 offset0:104 offset1:106
	s_waitcnt lgkmcnt(7)
	v_mfma_f32_32x32x16_bf16 v[68:83], v[172:175], v[144:147], v[68:83]
	v_add_u32_e32 v172, 0x6000, v190
	ds_read2_b64 v[172:175], v172 offset0:108 offset1:110
	v_add_u32_e32 v88, 0x6000, v190
	s_waitcnt lgkmcnt(3)
	v_mfma_f32_32x32x16_bf16 v[84:99], v[84:87], v[116:119], 0
	v_add_u32_e32 v116, v159, v153
	v_add_u32_e32 v116, 0x8000, v116
	ds_read2_b64 v[116:119], v116 offset0:128 offset1:130
	s_waitcnt lgkmcnt(3)
	v_mfma_f32_32x32x16_bf16 v[84:99], v[164:167], v[120:123], v[84:99]
	v_add_u32_e32 v120, v159, v153
	v_add_u32_e32 v120, 0x8000, v120
	ds_read2_b64 v[120:123], v120 offset0:132 offset1:134
	s_waitcnt lgkmcnt(3)
	v_mfma_f32_32x32x16_bf16 v[84:99], v[168:171], v[124:127], v[84:99]
	v_add_u32_e32 v124, v159, v153
	v_add_u32_e32 v124, 0x8000, v124
	ds_read2_b64 v[124:127], v124 offset0:136 offset1:138
	s_waitcnt lgkmcnt(3)
	v_mfma_f32_32x32x16_bf16 v[84:99], v[172:175], v[128:131], v[84:99]
	v_add_u32_e32 v128, v159, v153
	v_add_u32_e32 v128, 0x8000, v128
	ds_read2_b64 v[128:131], v128 offset0:140 offset1:142
	v_mfma_f32_32x32x16_bf16 v[84:99], v[176:179], v[132:135], v[84:99]
	v_add_u32_e32 v132, v159, v153
	v_add_u32_e32 v132, 0x9000, v132
	ds_read2_b64 v[132:135], v132 offset0:160 offset1:162
	v_mfma_f32_32x32x16_bf16 v[84:99], v[180:183], v[136:139], v[84:99]
	v_add_u32_e32 v136, v159, v153
	v_add_u32_e32 v136, 0x9000, v136
	ds_read2_b64 v[136:139], v136 offset0:164 offset1:166
	v_mfma_f32_32x32x16_bf16 v[84:99], v[184:187], v[140:143], v[84:99]
	v_add_u32_e32 v140, v159, v153
	v_add_u32_e32 v140, 0x9000, v140
	ds_read2_b64 v[140:143], v140 offset0:168 offset1:170
	v_mfma_f32_32x32x16_bf16 v[84:99], v[194:197], v[144:147], v[84:99]
	v_add_u32_e32 v144, v159, v153
	v_add_u32_e32 v144, 0x9000, v144
	ds_read2_b64 v[144:147], v144 offset0:172 offset1:174
	v_add_u32_e32 v159, v159, v153
	v_lshl_add_u64 v[182:183], s[6:7], 0, v[162:163]
	s_add_i32 s35, s35, 1
	s_add_u32 s26, s6, s28
	s_addc_u32 s27, s7, s29
	v_mov_b64_e32 v[232:233], s[26:27]
	global_load_dword v201, v[232:233], off
	s_waitcnt lgkmcnt(7)
	v_mfma_f32_32x32x16_bf16 v[68:83], v[116:119], v[100:103], v[68:83]
	s_mov_b64 s[26:27], 0x41a20000
	v_lshl_add_u64 v[218:219], v[182:183], 0, s[26:27]
	s_mov_b64 s[26:27], 0x41a21000
	v_lshl_add_u64 v[220:221], v[182:183], 0, s[26:27]
	global_load_dword v166, v[218:219], off
	global_load_dword v167, v[218:219], off offset:2048
	global_load_dword v164, v[220:221], off
	global_load_dword v165, v[220:221], off offset:2048
	s_waitcnt lgkmcnt(3)
	v_mfma_f32_32x32x16_bf16 v[84:99], v[132:135], v[100:103], v[84:99]
	s_mov_b64 s[26:27], 0x41a24000
	v_lshl_add_u64 v[222:223], v[182:183], 0, s[26:27]
	s_mov_b64 s[26:27], 0x41a25000
	v_lshl_add_u64 v[224:225], v[182:183], 0, s[26:27]
	global_load_dword v168, v[222:223], off
	global_load_dword v169, v[222:223], off offset:2048
	global_load_dword v170, v[224:225], off
	global_load_dword v171, v[224:225], off offset:2048
	v_mfma_f32_32x32x16_bf16 v[68:83], v[120:123], v[104:107], v[68:83]
	s_mov_b64 s[26:27], 0x41a28000
	v_lshl_add_u64 v[218:219], v[182:183], 0, s[26:27]
	s_mov_b64 s[26:27], 0x41a29000
	v_lshl_add_u64 v[220:221], v[182:183], 0, s[26:27]
	global_load_dword v180, v[218:219], off
	global_load_dword v181, v[218:219], off offset:2048
	global_load_dword v194, v[220:221], off
	global_load_dword v195, v[220:221], off offset:2048
	s_waitcnt lgkmcnt(2)
	v_mfma_f32_32x32x16_bf16 v[84:99], v[136:139], v[104:107], v[84:99]
	s_mov_b64 s[26:27], 0x41a2c000
	v_lshl_add_u64 v[222:223], v[182:183], 0, s[26:27]
	s_mov_b64 s[26:27], 0x41a2d000
	v_lshl_add_u64 v[224:225], v[182:183], 0, s[26:27]
	global_load_dword v196, v[222:223], off
	global_load_dword v197, v[222:223], off offset:2048
	global_load_dword v198, v[224:225], off
	global_load_dword v199, v[224:225], off offset:2048
	v_mfma_f32_32x32x16_bf16 v[68:83], v[124:127], v[108:111], v[68:83]
	s_mov_b64 s[26:27], 0x41a30000
	v_lshl_add_u64 v[218:219], v[182:183], 0, s[26:27]
	s_mov_b64 s[26:27], 0x41a31000
	v_lshl_add_u64 v[220:221], v[182:183], 0, s[26:27]
	global_load_dword v172, v[218:219], off
	global_load_dword v173, v[218:219], off offset:2048
	global_load_dword v174, v[220:221], off
	global_load_dword v175, v[220:221], off offset:2048
	s_waitcnt lgkmcnt(1)
	v_mfma_f32_32x32x16_bf16 v[84:99], v[140:143], v[108:111], v[84:99]
	s_mov_b64 s[26:27], 0x41a34000
	v_lshl_add_u64 v[222:223], v[182:183], 0, s[26:27]
	s_mov_b64 s[26:27], 0x41a35000
	v_lshl_add_u64 v[224:225], v[182:183], 0, s[26:27]
	global_load_dword v176, v[222:223], off
	global_load_dword v177, v[222:223], off offset:2048
	global_load_dword v178, v[224:225], off
	global_load_dword v179, v[224:225], off offset:2048
	v_mfma_f32_32x32x16_bf16 v[68:83], v[128:131], v[112:115], v[68:83]
	s_mov_b64 s[26:27], 0x41a38000
	v_lshl_add_u64 v[218:219], v[182:183], 0, s[26:27]
	s_mov_b64 s[26:27], 0x41a39000
	v_lshl_add_u64 v[220:221], v[182:183], 0, s[26:27]
	global_load_dword v202, v[218:219], off
	global_load_dword v203, v[218:219], off offset:2048
	global_load_dword v204, v[220:221], off
	global_load_dword v205, v[220:221], off offset:2048
	s_waitcnt lgkmcnt(0)
	v_mfma_f32_32x32x16_bf16 v[84:99], v[144:147], v[112:115], v[84:99]
	s_mov_b64 s[26:27], 0x41a3c000
	v_lshl_add_u64 v[222:223], v[182:183], 0, s[26:27]
	s_mov_b64 s[26:27], 0x41a3d000
	v_lshl_add_u64 v[224:225], v[182:183], 0, s[26:27]
	global_load_dword v206, v[222:223], off
	global_load_dword v207, v[222:223], off offset:2048
	global_load_dword v208, v[224:225], off
	global_load_dword v209, v[224:225], off offset:2048
	v_add_u32_e32 v116, 0xa000, v159
	ds_read2_b64 v[116:119], v116 offset0:192 offset1:194
	v_add_u32_e32 v120, 0xa000, v159
	ds_read2_b64 v[120:123], v120 offset0:196 offset1:198
	v_add_u32_e32 v124, 0xa000, v159
	ds_read2_b64 v[124:127], v124 offset0:200 offset1:202
	v_add_u32_e32 v128, 0xa000, v159
	ds_read2_b64 v[128:131], v128 offset0:204 offset1:206
	v_add_u32_e32 v132, 0xb000, v159
	ds_read2_b64 v[132:135], v132 offset0:224 offset1:226
	v_add_u32_e32 v136, 0xb000, v159
	ds_read2_b64 v[136:139], v136 offset0:228 offset1:230
	v_add_u32_e32 v140, 0xb000, v159
	ds_read2_b64 v[140:143], v140 offset0:232 offset1:234
	v_add_u32_e32 v144, 0xb000, v159
	ds_read2_b64 v[144:147], v144 offset0:236 offset1:238
	v_pk_mul_f32 v[66:67], v[66:67], v[200:201] op_sel_hi:[1,0]
	v_pk_mul_f32 v[64:65], v[64:65], v[200:201] op_sel_hi:[1,0]
	v_pk_mul_f32 v[62:63], v[62:63], v[200:201] op_sel_hi:[1,0]
	v_pk_mul_f32 v[60:61], v[60:61], v[200:201] op_sel_hi:[1,0]
	v_pk_mul_f32 v[58:59], v[58:59], v[200:201] op_sel_hi:[1,0]
	v_pk_mul_f32 v[56:57], v[56:57], v[200:201] op_sel_hi:[1,0]
	v_pk_mul_f32 v[54:55], v[54:55], v[200:201] op_sel_hi:[1,0]
	v_pk_mul_f32 v[52:53], v[52:53], v[200:201] op_sel_hi:[1,0]
	v_pk_mul_f32 v[50:51], v[50:51], v[200:201] op_sel_hi:[1,0]
	v_pk_mul_f32 v[48:49], v[48:49], v[200:201] op_sel_hi:[1,0]
	v_pk_mul_f32 v[46:47], v[46:47], v[200:201] op_sel_hi:[1,0]
	v_pk_mul_f32 v[44:45], v[44:45], v[200:201] op_sel_hi:[1,0]
	v_pk_mul_f32 v[42:43], v[42:43], v[200:201] op_sel_hi:[1,0]
	v_pk_mul_f32 v[40:41], v[40:41], v[200:201] op_sel_hi:[1,0]
	v_pk_mul_f32 v[38:39], v[38:39], v[200:201] op_sel_hi:[1,0]
	v_pk_mul_f32 v[36:37], v[36:37], v[200:201] op_sel_hi:[1,0]
	s_waitcnt lgkmcnt(0)
	v_mfma_f32_32x32x16_bf16 v[52:67], v[116:119], v[100:103], v[52:67]
	s_mov_b64 s[26:27], 0x47200000
	v_lshl_add_u64 v[218:219], v[182:183], 0, s[26:27]
	global_store_dword v[218:219], v68, off
	global_store_dword v[218:219], v69, off offset:2048
	v_mfma_f32_32x32x16_bf16 v[36:51], v[132:135], v[100:103], v[36:51]
	s_mov_b64 s[26:27], 0x47201000
	v_lshl_add_u64 v[220:221], v[182:183], 0, s[26:27]
	global_store_dword v[220:221], v70, off
	global_store_dword v[220:221], v71, off offset:2048
	v_mfma_f32_32x32x16_bf16 v[52:67], v[120:123], v[104:107], v[52:67]
	s_mov_b64 s[26:27], 0x47204000
	v_lshl_add_u64 v[222:223], v[182:183], 0, s[26:27]
	global_store_dword v[222:223], v72, off
	global_store_dword v[222:223], v73, off offset:2048
	v_mfma_f32_32x32x16_bf16 v[36:51], v[136:139], v[104:107], v[36:51]
	s_mov_b64 s[26:27], 0x47205000
	v_lshl_add_u64 v[224:225], v[182:183], 0, s[26:27]
	global_store_dword v[224:225], v74, off
	global_store_dword v[224:225], v75, off offset:2048
	v_mfma_f32_32x32x16_bf16 v[52:67], v[124:127], v[108:111], v[52:67]
	s_mov_b64 s[26:27], 0x47208000
	v_lshl_add_u64 v[218:219], v[182:183], 0, s[26:27]
	global_store_dword v[218:219], v76, off
	global_store_dword v[218:219], v77, off offset:2048
	v_mfma_f32_32x32x16_bf16 v[36:51], v[140:143], v[108:111], v[36:51]
	s_mov_b64 s[26:27], 0x47209000
	v_lshl_add_u64 v[220:221], v[182:183], 0, s[26:27]
	global_store_dword v[220:221], v78, off
	global_store_dword v[220:221], v79, off offset:2048
	v_mfma_f32_32x32x16_bf16 v[52:67], v[128:131], v[112:115], v[52:67]
	s_mov_b64 s[26:27], 0x4720c000
	v_lshl_add_u64 v[222:223], v[182:183], 0, s[26:27]
	global_store_dword v[222:223], v80, off
	global_store_dword v[222:223], v81, off offset:2048
	v_mfma_f32_32x32x16_bf16 v[36:51], v[144:147], v[112:115], v[36:51]
	s_mov_b64 s[26:27], 0x4720d000
	v_lshl_add_u64 v[224:225], v[182:183], 0, s[26:27]
	global_store_dword v[224:225], v82, off
	global_store_dword v[224:225], v83, off offset:2048
	v_add_u32_e32 v116, 0xc800, v159
	ds_read2_b64 v[116:119], v116 offset1:2
	v_add_u32_e32 v120, 0xc800, v159
	ds_read2_b64 v[120:123], v120 offset0:4 offset1:6
	v_add_u32_e32 v124, 0xc800, v159
	ds_read2_b64 v[124:127], v124 offset0:8 offset1:10
	v_add_u32_e32 v128, 0xc800, v159
	ds_read2_b64 v[128:131], v128 offset0:12 offset1:14
	v_add_u32_e32 v132, 0xd800, v159
	ds_read2_b64 v[132:135], v132 offset0:32 offset1:34
	v_add_u32_e32 v136, 0xd800, v159
	ds_read2_b64 v[136:139], v136 offset0:36 offset1:38
	v_add_u32_e32 v140, 0xd800, v159
	ds_read2_b64 v[140:143], v140 offset0:40 offset1:42
	v_add_u32_e32 v144, 0xd800, v159
	ds_read2_b64 v[144:147], v144 offset0:44 offset1:46
	v_pk_mul_f32 v[34:35], v[34:35], v[200:201] op_sel_hi:[1,0]
	v_pk_mul_f32 v[32:33], v[32:33], v[200:201] op_sel_hi:[1,0]
	v_pk_mul_f32 v[30:31], v[30:31], v[200:201] op_sel_hi:[1,0]
	v_pk_mul_f32 v[28:29], v[28:29], v[200:201] op_sel_hi:[1,0]
	v_pk_mul_f32 v[26:27], v[26:27], v[200:201] op_sel_hi:[1,0]
	v_pk_mul_f32 v[24:25], v[24:25], v[200:201] op_sel_hi:[1,0]
	v_pk_mul_f32 v[22:23], v[22:23], v[200:201] op_sel_hi:[1,0]
	v_pk_mul_f32 v[20:21], v[20:21], v[200:201] op_sel_hi:[1,0]
	v_pk_mul_f32 v[18:19], v[18:19], v[200:201] op_sel_hi:[1,0]
	v_pk_mul_f32 v[16:17], v[16:17], v[200:201] op_sel_hi:[1,0]
	v_pk_mul_f32 v[14:15], v[14:15], v[200:201] op_sel_hi:[1,0]
	v_pk_mul_f32 v[12:13], v[12:13], v[200:201] op_sel_hi:[1,0]
	v_pk_mul_f32 v[10:11], v[10:11], v[200:201] op_sel_hi:[1,0]
	v_pk_mul_f32 v[8:9], v[8:9], v[200:201] op_sel_hi:[1,0]
	v_pk_mul_f32 v[6:7], v[6:7], v[200:201] op_sel_hi:[1,0]
	v_pk_mul_f32 v[4:5], v[4:5], v[200:201] op_sel_hi:[1,0]
	s_waitcnt lgkmcnt(0)
	v_mfma_f32_32x32x16_bf16 v[20:35], v[116:119], v[100:103], v[20:35]
	s_mov_b64 s[26:27], 0x47210000
	v_lshl_add_u64 v[218:219], v[182:183], 0, s[26:27]
	global_store_dword v[218:219], v84, off
	global_store_dword v[218:219], v85, off offset:2048
	v_mfma_f32_32x32x16_bf16 v[4:19], v[132:135], v[100:103], v[4:19]
	s_mov_b64 s[26:27], 0x47211000
	v_lshl_add_u64 v[220:221], v[182:183], 0, s[26:27]
	global_store_dword v[220:221], v86, off
	global_store_dword v[220:221], v87, off offset:2048
	v_mfma_f32_32x32x16_bf16 v[20:35], v[120:123], v[104:107], v[20:35]
	s_mov_b64 s[26:27], 0x47214000
	v_lshl_add_u64 v[222:223], v[182:183], 0, s[26:27]
	global_store_dword v[222:223], v88, off
	global_store_dword v[222:223], v89, off offset:2048
	v_mfma_f32_32x32x16_bf16 v[4:19], v[136:139], v[104:107], v[4:19]
	s_mov_b64 s[26:27], 0x47215000
	v_lshl_add_u64 v[224:225], v[182:183], 0, s[26:27]
	global_store_dword v[224:225], v90, off
	global_store_dword v[224:225], v91, off offset:2048
	v_mfma_f32_32x32x16_bf16 v[20:35], v[124:127], v[108:111], v[20:35]
	s_mov_b64 s[26:27], 0x47218000
	v_lshl_add_u64 v[218:219], v[182:183], 0, s[26:27]
	global_store_dword v[218:219], v92, off
	global_store_dword v[218:219], v93, off offset:2048
	v_mfma_f32_32x32x16_bf16 v[4:19], v[140:143], v[108:111], v[4:19]
	s_mov_b64 s[26:27], 0x47219000
	v_lshl_add_u64 v[220:221], v[182:183], 0, s[26:27]
	global_store_dword v[220:221], v94, off
	global_store_dword v[220:221], v95, off offset:2048
	v_mfma_f32_32x32x16_bf16 v[20:35], v[128:131], v[112:115], v[20:35]
	s_mov_b64 s[26:27], 0x4721c000
	v_lshl_add_u64 v[222:223], v[182:183], 0, s[26:27]
	global_store_dword v[222:223], v96, off
	global_store_dword v[222:223], v97, off offset:2048
	v_mfma_f32_32x32x16_bf16 v[4:19], v[144:147], v[112:115], v[4:19]
	s_mov_b64 s[26:27], 0x4721d000
	v_lshl_add_u64 v[224:225], v[182:183], 0, s[26:27]
	global_store_dword v[224:225], v98, off
	global_store_dword v[224:225], v99, off offset:2048
	s_add_u32 s28, s28, 4
	s_addc_u32 s29, s29, 0
	v_lshl_add_u64 v[162:163], v[162:163], 0, s[38:39]
	s_cmp_eq_u32 s35, 63
	s_barrier
	s_cbranch_scc0 .LBB0_490
	s_waitcnt vmcnt(32)
	v_add_u32_e32 v82, v157, v155
	v_cvt_pk_bf16_f32 v52, v52, v53
	v_cvt_pk_bf16_f32 v53, v54, v55
	v_cvt_pk_bf16_f32 v54, v56, v57
	v_cvt_pk_bf16_f32 v57, v62, v63
	v_cvt_pk_bf16_f32 v62, v8, v9
	v_add_u32_e32 v8, 0xe800, v82
	v_cvt_pk_bf16_f32 v56, v60, v61
	v_cvt_pk_bf16_f32 v36, v36, v37
	v_cvt_pk_bf16_f32 v37, v38, v39
	v_cvt_pk_bf16_f32 v38, v40, v41
	v_cvt_pk_bf16_f32 v39, v42, v43
	v_cvt_pk_bf16_f32 v40, v44, v45
	v_cvt_pk_bf16_f32 v41, v46, v47
	v_cvt_pk_bf16_f32 v42, v48, v49
	v_cvt_pk_bf16_f32 v43, v50, v51
	v_cvt_pk_bf16_f32 v44, v20, v21
	v_cvt_pk_bf16_f32 v45, v22, v23
	v_cvt_pk_bf16_f32 v46, v24, v25
	v_cvt_pk_bf16_f32 v47, v26, v27
	v_cvt_pk_bf16_f32 v48, v28, v29
	v_cvt_pk_bf16_f32 v49, v30, v31
	v_cvt_pk_bf16_f32 v50, v32, v33
	v_cvt_pk_bf16_f32 v51, v34, v35
	v_cvt_pk_bf16_f32 v60, v4, v5
	v_cvt_pk_bf16_f32 v61, v6, v7
	ds_read2_b64 v[4:7], v8 offset0:64 offset1:66
	ds_read2_b64 v[20:23], v8 offset0:68 offset1:70
	ds_read2_b64 v[24:27], v8 offset0:72 offset1:74
	ds_read2_b64 v[28:31], v8 offset0:76 offset1:78
	ds_read2_b64 v[32:35], v8 offset0:80 offset1:82
	ds_read2_b64 v[68:71], v8 offset0:84 offset1:86
	ds_read2_b64 v[72:75], v8 offset0:88 offset1:90
	ds_read2_b64 v[78:81], v8 offset0:92 offset1:94
	s_add_u32 s24, s6, s24
	s_addc_u32 s25, s7, s25
	s_add_u32 s24, s24, s9
	s_addc_u32 s25, s25, 0
	v_lshl_add_u64 v[76:77], v[160:161], 2, s[24:25]
	v_cvt_pk_bf16_f32 v55, v58, v59
	v_cvt_pk_bf16_f32 v58, v64, v65
	v_cvt_pk_bf16_f32 v59, v66, v67
	v_cvt_pk_bf16_f32 v63, v10, v11
	v_cvt_pk_bf16_f32 v64, v12, v13
	v_cvt_pk_bf16_f32 v65, v14, v15
	v_cvt_pk_bf16_f32 v66, v16, v17
	v_cvt_pk_bf16_f32 v67, v18, v19
	s_waitcnt lgkmcnt(7)
	v_mfma_f32_32x32x16_bf16 v[4:19], v[4:7], v[52:55], 0
	s_waitcnt lgkmcnt(6)
	v_mfma_f32_32x32x16_bf16 v[4:19], v[20:23], v[56:59], v[4:19]
	s_waitcnt lgkmcnt(5)
	v_mfma_f32_32x32x16_bf16 v[4:19], v[24:27], v[36:39], v[4:19]
	s_waitcnt lgkmcnt(4)
	v_mfma_f32_32x32x16_bf16 v[4:19], v[28:31], v[40:43], v[4:19]
	s_waitcnt lgkmcnt(3)
	v_mfma_f32_32x32x16_bf16 v[4:19], v[32:35], v[44:47], v[4:19]
	s_waitcnt lgkmcnt(2)
	v_mfma_f32_32x32x16_bf16 v[4:19], v[68:71], v[48:51], v[4:19]
	s_waitcnt lgkmcnt(1)
	v_mfma_f32_32x32x16_bf16 v[4:19], v[72:75], v[60:63], v[4:19]
	s_waitcnt lgkmcnt(0)
	v_mfma_f32_32x32x16_bf16 v[4:19], v[78:81], v[64:67], v[4:19]
	v_add_u32_e32 v20, 0x2100, v82
	v_add_u32_e32 v24, 0xe800, v20
	ds_read2_b64 v[20:23], v24 offset0:64 offset1:66
	ds_read2_b64 v[68:71], v24 offset0:68 offset1:70
	ds_read2_b64 v[72:75], v24 offset0:72 offset1:74
	ds_read2_b64 v[78:81], v24 offset0:76 offset1:78
	ds_read2_b64 v[82:85], v24 offset0:80 offset1:82
	ds_read2_b64 v[86:89], v24 offset0:84 offset1:86
	ds_read2_b64 v[90:93], v24 offset0:88 offset1:90
	ds_read2_b64 v[94:97], v24 offset0:92 offset1:94
	s_waitcnt lgkmcnt(7)
	v_mfma_f32_32x32x16_bf16 v[20:35], v[20:23], v[52:55], 0
	s_waitcnt lgkmcnt(6)
	v_mfma_f32_32x32x16_bf16 v[20:35], v[68:71], v[56:59], v[20:35]
	s_waitcnt lgkmcnt(5)
	v_mfma_f32_32x32x16_bf16 v[20:35], v[72:75], v[36:39], v[20:35]
	s_waitcnt lgkmcnt(4)
	v_mfma_f32_32x32x16_bf16 v[20:35], v[78:81], v[40:43], v[20:35]
	s_waitcnt lgkmcnt(3)
	v_mfma_f32_32x32x16_bf16 v[20:35], v[82:85], v[44:47], v[20:35]
	s_waitcnt lgkmcnt(2)
	v_mfma_f32_32x32x16_bf16 v[20:35], v[86:89], v[48:51], v[20:35]
	s_waitcnt lgkmcnt(1)
	v_mfma_f32_32x32x16_bf16 v[20:35], v[90:93], v[60:63], v[20:35]
	s_waitcnt lgkmcnt(0)
	v_mfma_f32_32x32x16_bf16 v[20:35], v[94:97], v[64:67], v[20:35]
	v_add_f32_e64 v4, v166, -v4
	v_add_f32_e64 v5, v167, -v5
	v_add_f32_e64 v6, v164, -v6
	v_add_f32_e64 v7, v165, -v7
	v_add_f32_e64 v8, v168, -v8
	v_add_f32_e64 v9, v169, -v9
	v_pk_add_f32 v[10:11], v[170:171], v[10:11] neg_lo:[0,1] neg_hi:[0,1]
	v_pk_add_f32 v[12:13], v[180:181], v[12:13] neg_lo:[0,1] neg_hi:[0,1]
	v_pk_add_f32 v[14:15], v[194:195], v[14:15] neg_lo:[0,1] neg_hi:[0,1]
	v_pk_add_f32 v[16:17], v[196:197], v[16:17] neg_lo:[0,1] neg_hi:[0,1]
	v_pk_add_f32 v[18:19], v[198:199], v[18:19] neg_lo:[0,1] neg_hi:[0,1]
	v_cvt_pk_bf16_f32 v68, v4, v5
	v_cvt_pk_bf16_f32 v69, v6, v7
	v_pk_add_f32 v[4:5], v[172:173], v[20:21] neg_lo:[0,1] neg_hi:[0,1]
	v_pk_add_f32 v[6:7], v[174:175], v[22:23] neg_lo:[0,1] neg_hi:[0,1]
	v_add3_u32 v98, s31, v149, v155
	v_cvt_pk_bf16_f32 v70, v8, v9
	v_cvt_pk_bf16_f32 v71, v10, v11
	v_cvt_pk_bf16_f32 v72, v12, v13
	v_cvt_pk_bf16_f32 v73, v14, v15
	v_cvt_pk_bf16_f32 v74, v16, v17
	v_cvt_pk_bf16_f32 v75, v18, v19
	v_pk_add_f32 v[8:9], v[176:177], v[24:25] neg_lo:[0,1] neg_hi:[0,1]
	v_pk_add_f32 v[10:11], v[178:179], v[26:27] neg_lo:[0,1] neg_hi:[0,1]
	v_pk_add_f32 v[12:13], v[202:203], v[28:29] neg_lo:[0,1] neg_hi:[0,1]
	v_pk_add_f32 v[14:15], v[204:205], v[30:31] neg_lo:[0,1] neg_hi:[0,1]
	v_pk_add_f32 v[16:17], v[206:207], v[32:33] neg_lo:[0,1] neg_hi:[0,1]
	v_pk_add_f32 v[18:19], v[208:209], v[34:35] neg_lo:[0,1] neg_hi:[0,1]
	v_cvt_pk_bf16_f32 v78, v4, v5
	v_cvt_pk_bf16_f32 v79, v6, v7
	ds_read2_b64 v[4:7], v98 offset1:2
	ds_read2_b64 v[20:23], v98 offset0:4 offset1:6
	ds_read2_b64 v[24:27], v98 offset0:8 offset1:10
	ds_read2_b64 v[28:31], v98 offset0:12 offset1:14
	ds_read2_b64 v[32:35], v98 offset0:16 offset1:18
	ds_read2_b64 v[82:85], v98 offset0:20 offset1:22
	ds_read2_b64 v[86:89], v98 offset0:24 offset1:26
	ds_read2_b64 v[90:93], v98 offset0:28 offset1:30
	v_cvt_pk_bf16_f32 v80, v8, v9
	v_cvt_pk_bf16_f32 v81, v10, v11
	v_cvt_pk_bf16_f32 v94, v12, v13
	v_cvt_pk_bf16_f32 v95, v14, v15
	v_cvt_pk_bf16_f32 v96, v16, v17
	v_cvt_pk_bf16_f32 v97, v18, v19
	s_waitcnt lgkmcnt(7)
	v_mfma_f32_32x32x16_bf16 v[4:19], v[4:7], v[52:55], 0
	s_waitcnt lgkmcnt(6)
	v_mfma_f32_32x32x16_bf16 v[4:19], v[20:23], v[56:59], v[4:19]
	s_waitcnt lgkmcnt(5)
	v_mfma_f32_32x32x16_bf16 v[4:19], v[24:27], v[36:39], v[4:19]
	s_waitcnt lgkmcnt(4)
	v_mfma_f32_32x32x16_bf16 v[4:19], v[28:31], v[40:43], v[4:19]
	s_waitcnt lgkmcnt(3)
	v_mfma_f32_32x32x16_bf16 v[4:19], v[32:35], v[44:47], v[4:19]
	s_waitcnt lgkmcnt(2)
	v_mfma_f32_32x32x16_bf16 v[4:19], v[82:85], v[48:51], v[4:19]
	s_waitcnt lgkmcnt(1)
	v_mfma_f32_32x32x16_bf16 v[4:19], v[86:89], v[60:63], v[4:19]
	s_waitcnt lgkmcnt(0)
	v_mfma_f32_32x32x16_bf16 v[4:19], v[90:93], v[64:67], v[4:19]
	v_add_u32_e32 v24, 0x2000, v98
	ds_read2_b64 v[20:23], v24 offset0:32 offset1:34
	ds_read2_b64 v[82:85], v24 offset0:36 offset1:38
	ds_read2_b64 v[86:89], v24 offset0:40 offset1:42
	ds_read2_b64 v[90:93], v24 offset0:44 offset1:46
	ds_read2_b64 v[98:101], v24 offset0:48 offset1:50
	ds_read2_b64 v[102:105], v24 offset0:52 offset1:54
	ds_read2_b64 v[106:109], v24 offset0:56 offset1:58
	ds_read2_b64 v[110:113], v24 offset0:60 offset1:62
	s_waitcnt lgkmcnt(7)
	v_mfma_f32_32x32x16_bf16 v[20:35], v[20:23], v[52:55], 0
	s_waitcnt lgkmcnt(6)
	v_mfma_f32_32x32x16_bf16 v[20:35], v[82:85], v[56:59], v[20:35]
	s_waitcnt lgkmcnt(5)
	v_mfma_f32_32x32x16_bf16 v[20:35], v[86:89], v[36:39], v[20:35]
	s_waitcnt lgkmcnt(4)
	v_mfma_f32_32x32x16_bf16 v[20:35], v[90:93], v[40:43], v[20:35]
	s_waitcnt lgkmcnt(3)
	v_mfma_f32_32x32x16_bf16 v[20:35], v[98:101], v[44:47], v[20:35]
	s_waitcnt lgkmcnt(2)
	v_mfma_f32_32x32x16_bf16 v[20:35], v[102:105], v[48:51], v[20:35]
	s_waitcnt lgkmcnt(1)
	v_mfma_f32_32x32x16_bf16 v[20:35], v[106:109], v[60:63], v[20:35]
	s_waitcnt lgkmcnt(0)
	v_mfma_f32_32x32x16_bf16 v[20:35], v[110:113], v[64:67], v[20:35]
	v_add3_u32 v52, s33, v149, v153
	v_add_u32_e32 v64, 0x1000, v52
	ds_read2_b64 v[36:39], v52 offset1:2
	ds_read2_b64 v[40:43], v52 offset0:4 offset1:6
	ds_read2_b64 v[44:47], v52 offset0:8 offset1:10
	ds_read2_b64 v[48:51], v52 offset0:12 offset1:14
	ds_read2_b64 v[52:55], v64 offset0:32 offset1:34
	ds_read2_b64 v[56:59], v64 offset0:36 offset1:38
	ds_read2_b64 v[60:63], v64 offset0:40 offset1:42
	ds_read2_b64 v[64:67], v64 offset0:44 offset1:46
	s_waitcnt lgkmcnt(7)
	v_mfma_f32_32x32x16_bf16 v[4:19], v[36:39], v[68:71], v[4:19]
	s_waitcnt lgkmcnt(3)
	v_mfma_f32_32x32x16_bf16 v[20:35], v[52:55], v[68:71], v[20:35]
	v_mfma_f32_32x32x16_bf16 v[4:19], v[40:43], v[72:75], v[4:19]
	s_waitcnt lgkmcnt(2)
	v_mfma_f32_32x32x16_bf16 v[20:35], v[56:59], v[72:75], v[20:35]
	v_mfma_f32_32x32x16_bf16 v[4:19], v[44:47], v[78:81], v[4:19]
	s_waitcnt lgkmcnt(1)
	v_mfma_f32_32x32x16_bf16 v[20:35], v[60:63], v[78:81], v[20:35]
	v_mfma_f32_32x32x16_bf16 v[4:19], v[48:51], v[94:97], v[4:19]
	s_waitcnt lgkmcnt(0)
	v_mfma_f32_32x32x16_bf16 v[20:35], v[64:67], v[94:97], v[20:35]
	v_lshl_add_u64 v[36:37], v[76:77], 0, v[2:3]
	s_mov_b32 s9, 0x479e0000
	v_add_co_u32_e32 v38, vcc, s9, v36
	s_mov_b32 s9, 0x479e1000
	s_nop 0
	v_addc_co_u32_e32 v39, vcc, 0, v37, vcc
	s_nop 3
	global_store_dword v[38:39], v4, off
	global_store_dword v[38:39], v5, off offset:2048
	v_add_co_u32_e32 v4, vcc, s9, v36
	s_mov_b32 s9, 0x479e4000
	s_nop 0
	v_addc_co_u32_e32 v5, vcc, 0, v37, vcc
	global_store_dword v[4:5], v6, off
	global_store_dword v[4:5], v7, off offset:2048
	v_add_co_u32_e32 v4, vcc, s9, v36
	s_mov_b32 s9, 0x479e5000
	s_nop 0
	v_addc_co_u32_e32 v5, vcc, 0, v37, vcc
	global_store_dword v[4:5], v8, off
	global_store_dword v[4:5], v9, off offset:2048
	v_add_co_u32_e32 v4, vcc, s9, v36
	s_mov_b32 s9, 0x479e8000
	s_nop 0
	v_addc_co_u32_e32 v5, vcc, 0, v37, vcc
	global_store_dword v[4:5], v10, off
	global_store_dword v[4:5], v11, off offset:2048
	v_add_co_u32_e32 v4, vcc, s9, v36
	s_mov_b32 s9, 0x479e9000
	s_nop 0
	v_addc_co_u32_e32 v5, vcc, 0, v37, vcc
	global_store_dword v[4:5], v12, off
	global_store_dword v[4:5], v13, off offset:2048
	v_add_co_u32_e32 v4, vcc, s9, v36
	s_mov_b32 s9, 0x479ec000
	s_nop 0
	v_addc_co_u32_e32 v5, vcc, 0, v37, vcc
	global_store_dword v[4:5], v14, off
	global_store_dword v[4:5], v15, off offset:2048
	v_add_co_u32_e32 v4, vcc, s9, v36
	s_mov_b32 s9, 0x479ed000
	s_nop 0
	v_addc_co_u32_e32 v5, vcc, 0, v37, vcc
	global_store_dword v[4:5], v16, off
	global_store_dword v[4:5], v17, off offset:2048
	v_add_co_u32_e32 v4, vcc, s9, v36
	s_mov_b32 s9, 0x479f0000
	s_nop 0
	v_addc_co_u32_e32 v5, vcc, 0, v37, vcc
	global_store_dword v[4:5], v18, off
	global_store_dword v[4:5], v19, off offset:2048
	v_add_co_u32_e32 v4, vcc, s9, v36
	s_mov_b32 s9, 0x479f1000
	s_nop 0
	v_addc_co_u32_e32 v5, vcc, 0, v37, vcc
	global_store_dword v[4:5], v20, off
	global_store_dword v[4:5], v21, off offset:2048
	v_add_co_u32_e32 v4, vcc, s9, v36
	s_mov_b32 s9, 0x479f4000
	s_nop 0
	v_addc_co_u32_e32 v5, vcc, 0, v37, vcc
	global_store_dword v[4:5], v22, off
	global_store_dword v[4:5], v23, off offset:2048
	v_add_co_u32_e32 v4, vcc, s9, v36
	s_mov_b32 s9, 0x479f5000
	s_nop 0
	v_addc_co_u32_e32 v5, vcc, 0, v37, vcc
	global_store_dword v[4:5], v24, off
	global_store_dword v[4:5], v25, off offset:2048
	v_add_co_u32_e32 v4, vcc, s9, v36
	s_mov_b32 s9, 0x479f8000
	s_nop 0
	v_addc_co_u32_e32 v5, vcc, 0, v37, vcc
	global_store_dword v[4:5], v26, off
	global_store_dword v[4:5], v27, off offset:2048
	v_add_co_u32_e32 v4, vcc, s9, v36
	s_mov_b32 s9, 0x479f9000
	s_nop 0
	v_addc_co_u32_e32 v5, vcc, 0, v37, vcc
	global_store_dword v[4:5], v28, off
	global_store_dword v[4:5], v29, off offset:2048
	v_add_co_u32_e32 v4, vcc, s9, v36
	s_mov_b32 s9, 0x479fc000
	s_nop 0
	v_addc_co_u32_e32 v5, vcc, 0, v37, vcc
	global_store_dword v[4:5], v30, off
	global_store_dword v[4:5], v31, off offset:2048
	v_add_co_u32_e32 v4, vcc, s9, v36
	s_nop 1
	v_addc_co_u32_e32 v5, vcc, 0, v37, vcc
	global_store_dword v[4:5], v32, off
	global_store_dword v[4:5], v33, off offset:2048
	v_add_co_u32_e32 v4, vcc, 0x479fd000, v36
	s_nop 1
	v_addc_co_u32_e32 v5, vcc, 0, v37, vcc
	global_store_dword v[4:5], v34, off
	global_store_dword v[4:5], v35, off offset:2048
	s_mov_b64 s[28:29], 0
	s_waitcnt lgkmcnt(0)
	s_barrier
